# v46 + placement: P3 alone shifted by 4 bytes (s_nop 0 at P3 entry and at P4 entry, P4..P9 phases unchanged)
# baseline (speedup 1.0000x reference)
; #define SEAM(k) do { if (IN(k) && IN((k) + 1)) xcd_barrier(bar); } while (0)
; __device__ __forceinline__ void p3_attention(Frame& F) {
;     const int c = blockIdx.x; if (c >= 256) return;
;     const int xcd = c & 7, j = c >> 3, bh = xcd * 2 + (j >> 4), qb = j & 15, b = bh >> 3, h = bh & 7;
; __global__ void __launch_bounds__(512, 2) fwd(Args args) {
;     ...
;     if (IN(3)) { p3_attention(F); } SEAM(3);
.LBB0_408:
	s_nop 0
	s_cmp_lt_i32 s34, 4
	s_cselect_b64 s[16:17], -1, 0
	s_cmpk_lt_i32 s2, 0x100
	s_cselect_b64 s[12:13], -1, 0
	s_and_b64 s[0:1], s[12:13], s[0:1]
	s_and_b64 s[0:1], s[16:17], s[0:1]
	s_andn2_b64 vcc, exec, s[0:1]
	s_cbranch_vccnz .LBB0_492
	v_readlane_b32 s99, v255, 8
	s_nop 3
	s_cmp_ge_u32 s99, 4
	s_cbranch_scc0 .Lp3_prio_done
	s_setprio 1
